# DPP reductions also in attention epilogue (counted LDS waits after removed shuffles made full waits)
# speedup vs baseline: 1.0052x; 1.0040x over previous
.LBB0_252:
	s_or_b64 exec, exec, s[6:7]
	s_waitcnt lgkmcnt(0)
	s_barrier
	ds_read_b128 v[32:35], v75 offset:1024
	ds_read_b128 v[36:39], v75 offset:1056
	v_lshlrev_b64 v[40:41], 11, v[110:111]
	v_lshl_add_u64 v[40:41], v[104:105], 0, v[40:41]
	s_add_i32 s15, s15, s84
	s_waitcnt lgkmcnt(0)
	v_mul_f32_e32 v0, v0, v32
	v_mul_f32_e32 v0, v69, v0
	v_cvt_pk_bf16_f32 v0, v0, s0
	global_store_short v[40:41], v0, off offset:512
	v_mul_f32_e32 v0, v16, v32
	v_mul_f32_e32 v0, v71, v0
	v_cvt_pk_bf16_f32 v0, v0, s0
	global_store_short v[40:41], v0, off offset:576
	v_mov_b32_e32 v41, s21
	v_or_b32_e32 v40, s20, v68
	v_mul_f32_e32 v0, v1, v33
	v_lshlrev_b64 v[40:41], 11, v[40:41]
	v_mul_f32_e32 v0, v69, v0
	v_lshl_add_u64 v[40:41], v[104:105], 0, v[40:41]
	v_cvt_pk_bf16_f32 v0, v0, s0
	global_store_short v[40:41], v0, off offset:512
	v_mul_f32_e32 v0, v17, v33
	v_mul_f32_e32 v0, v71, v0
	v_cvt_pk_bf16_f32 v0, v0, s0
	global_store_short v[40:41], v0, off offset:576
	v_mov_b32_e32 v1, s21
	v_or_b32_e32 v0, s20, v70
	v_mul_f32_e32 v2, v2, v34
	v_lshlrev_b64 v[0:1], 11, v[0:1]
	v_mul_f32_e32 v2, v69, v2
	v_lshl_add_u64 v[0:1], v[104:105], 0, v[0:1]
	v_cvt_pk_bf16_f32 v2, v2, s0
	global_store_short v[0:1], v2, off offset:512
	v_mul_f32_e32 v2, v18, v34
	v_mul_f32_e32 v2, v71, v2
	v_cvt_pk_bf16_f32 v2, v2, s0
	global_store_short v[0:1], v2, off offset:576
	v_mov_b32_e32 v1, s21
	v_or_b32_e32 v0, s20, v72
	v_mul_f32_e32 v2, v3, v35
	v_lshlrev_b64 v[0:1], 11, v[0:1]
	v_mul_f32_e32 v2, v69, v2
	v_lshl_add_u64 v[0:1], v[104:105], 0, v[0:1]
	v_cvt_pk_bf16_f32 v2, v2, s0
	global_store_short v[0:1], v2, off offset:512
	v_mul_f32_e32 v2, v19, v35
	v_mul_f32_e32 v2, v71, v2
	v_cvt_pk_bf16_f32 v2, v2, s0
	global_store_short v[0:1], v2, off offset:576
	v_mov_b32_e32 v1, s21
	v_or_b32_e32 v0, s20, v74
	s_waitcnt lgkmcnt(0)
	v_mul_f32_e32 v2, v4, v36
	v_lshlrev_b64 v[0:1], 11, v[0:1]
	v_mul_f32_e32 v2, v69, v2
	v_lshl_add_u64 v[0:1], v[104:105], 0, v[0:1]
	v_cvt_pk_bf16_f32 v2, v2, s0
	global_store_short v[0:1], v2, off offset:512
	v_mul_f32_e32 v2, v20, v36
	v_mul_f32_e32 v2, v71, v2
	v_cvt_pk_bf16_f32 v2, v2, s0
	global_store_short v[0:1], v2, off offset:576
	v_mov_b32_e32 v1, s21
	v_or_b32_e32 v0, s20, v76
	v_mul_f32_e32 v2, v5, v37
	v_lshlrev_b64 v[0:1], 11, v[0:1]
	v_mul_f32_e32 v2, v69, v2
	v_lshl_add_u64 v[0:1], v[104:105], 0, v[0:1]
	v_cvt_pk_bf16_f32 v2, v2, s0
	global_store_short v[0:1], v2, off offset:512
	v_mul_f32_e32 v2, v21, v37
	v_mul_f32_e32 v2, v71, v2
	v_cvt_pk_bf16_f32 v2, v2, s0
	global_store_short v[0:1], v2, off offset:576
	v_mov_b32_e32 v1, s21
	v_or_b32_e32 v0, s20, v78
	v_mul_f32_e32 v2, v6, v38
	v_lshlrev_b64 v[0:1], 11, v[0:1]
	v_mul_f32_e32 v2, v69, v2
	v_lshl_add_u64 v[0:1], v[104:105], 0, v[0:1]
	v_cvt_pk_bf16_f32 v2, v2, s0
	global_store_short v[0:1], v2, off offset:512
	v_mul_f32_e32 v2, v22, v38
	v_mul_f32_e32 v2, v71, v2
	v_cvt_pk_bf16_f32 v2, v2, s0
	global_store_short v[0:1], v2, off offset:576
	v_mov_b32_e32 v1, s21
	v_or_b32_e32 v0, s20, v80
	v_mul_f32_e32 v2, v7, v39
	v_lshlrev_b64 v[0:1], 11, v[0:1]
	v_mul_f32_e32 v2, v69, v2
	v_lshl_add_u64 v[0:1], v[104:105], 0, v[0:1]
	v_cvt_pk_bf16_f32 v2, v2, s0
	global_store_short v[0:1], v2, off offset:512
	v_mul_f32_e32 v2, v23, v39
	v_mul_f32_e32 v2, v71, v2
	v_cvt_pk_bf16_f32 v2, v2, s0
	global_store_short v[0:1], v2, off offset:576
	ds_read_b128 v[0:3], v75 offset:1088
	ds_read_b128 v[4:7], v75 offset:1120
	v_mov_b32_e32 v17, s21
	v_or_b32_e32 v16, s20, v82
	v_lshlrev_b64 v[16:17], 11, v[16:17]
	s_waitcnt lgkmcnt(0)
	v_mul_f32_e32 v8, v8, v0
	v_mul_f32_e32 v0, v24, v0
	v_mul_f32_e32 v8, v69, v8
	v_mul_f32_e32 v0, v71, v0
	v_lshl_add_u64 v[16:17], v[104:105], 0, v[16:17]
	v_cvt_pk_bf16_f32 v8, v8, s0
	v_cvt_pk_bf16_f32 v0, v0, s0
	global_store_short v[16:17], v8, off offset:512
	global_store_short v[16:17], v0, off offset:576
	v_mov_b32_e32 v17, s21
	v_or_b32_e32 v16, s20, v84
	v_mul_f32_e32 v0, v9, v1
	v_lshlrev_b64 v[16:17], 11, v[16:17]
	v_mul_f32_e32 v0, v69, v0
	v_lshl_add_u64 v[16:17], v[104:105], 0, v[16:17]
	v_cvt_pk_bf16_f32 v0, v0, s0
	global_store_short v[16:17], v0, off offset:512
	v_mul_f32_e32 v0, v25, v1
	v_mul_f32_e32 v0, v71, v0
	v_cvt_pk_bf16_f32 v0, v0, s0
	global_store_short v[16:17], v0, off offset:576
	v_mov_b32_e32 v1, s21
	v_or_b32_e32 v0, s20, v86
	v_mul_f32_e32 v8, v10, v2
	v_mul_f32_e32 v2, v26, v2
	v_lshlrev_b64 v[0:1], 11, v[0:1]
	v_mul_f32_e32 v8, v69, v8
	v_mul_f32_e32 v2, v71, v2
	v_lshl_add_u64 v[0:1], v[104:105], 0, v[0:1]
	v_cvt_pk_bf16_f32 v8, v8, s0
	v_cvt_pk_bf16_f32 v2, v2, s0
	global_store_short v[0:1], v8, off offset:512
	global_store_short v[0:1], v2, off offset:576
	v_mov_b32_e32 v1, s21
	v_or_b32_e32 v0, s20, v88
	v_mul_f32_e32 v2, v11, v3
	v_lshlrev_b64 v[0:1], 11, v[0:1]
	v_mul_f32_e32 v2, v69, v2
	v_lshl_add_u64 v[0:1], v[104:105], 0, v[0:1]
	v_cvt_pk_bf16_f32 v2, v2, s0
	global_store_short v[0:1], v2, off offset:512
	v_mul_f32_e32 v2, v27, v3
	v_mul_f32_e32 v2, v71, v2
	v_cvt_pk_bf16_f32 v2, v2, s0
	global_store_short v[0:1], v2, off offset:576
	v_mov_b32_e32 v1, s21
	v_or_b32_e32 v0, s20, v90
	s_waitcnt lgkmcnt(0)
	v_mul_f32_e32 v2, v12, v4
	v_lshlrev_b64 v[0:1], 11, v[0:1]
	v_mul_f32_e32 v2, v69, v2
	v_lshl_add_u64 v[0:1], v[104:105], 0, v[0:1]
	v_cvt_pk_bf16_f32 v2, v2, s0
	global_store_short v[0:1], v2, off offset:512
	v_mul_f32_e32 v2, v28, v4
	v_mul_f32_e32 v2, v71, v2
	v_cvt_pk_bf16_f32 v2, v2, s0
	global_store_short v[0:1], v2, off offset:576
	v_mov_b32_e32 v1, s21
	v_or_b32_e32 v0, s20, v92
	v_mul_f32_e32 v2, v13, v5
	v_lshlrev_b64 v[0:1], 11, v[0:1]
	v_mul_f32_e32 v2, v69, v2
	v_lshl_add_u64 v[0:1], v[104:105], 0, v[0:1]
	v_cvt_pk_bf16_f32 v2, v2, s0
	global_store_short v[0:1], v2, off offset:512
	v_mul_f32_e32 v2, v29, v5
	v_mul_f32_e32 v2, v71, v2
	v_cvt_pk_bf16_f32 v2, v2, s0
	global_store_short v[0:1], v2, off offset:576
	v_mov_b32_e32 v1, s21
	v_or_b32_e32 v0, s20, v94
	v_mul_f32_e32 v2, v14, v6
	v_lshlrev_b64 v[0:1], 11, v[0:1]
	v_mul_f32_e32 v2, v69, v2
	v_lshl_add_u64 v[0:1], v[104:105], 0, v[0:1]
	v_cvt_pk_bf16_f32 v2, v2, s0
	global_store_short v[0:1], v2, off offset:512
	v_mul_f32_e32 v2, v30, v6
	v_mul_f32_e32 v2, v71, v2
	v_cvt_pk_bf16_f32 v2, v2, s0
	global_store_short v[0:1], v2, off offset:576
	v_mov_b32_e32 v1, s21
	v_or_b32_e32 v0, s20, v96
	v_mul_f32_e32 v2, v15, v7
	v_lshlrev_b64 v[0:1], 11, v[0:1]
	v_mul_f32_e32 v2, v69, v2
	v_lshl_add_u64 v[0:1], v[104:105], 0, v[0:1]
	v_cvt_pk_bf16_f32 v2, v2, s0
	global_store_short v[0:1], v2, off offset:512
	v_mul_f32_e32 v2, v31, v7
	v_mul_f32_e32 v2, v71, v2
	s_add_i32 s14, s14, s23
	v_cvt_pk_bf16_f32 v2, v2, s0
	s_cmpk_lt_i32 s15, 0x200
	global_store_short v[0:1], v2, off offset:576
	s_cbranch_scc0 .LBB0_260
.LBB0_253:
	s_ashr_i32 s6, s15, 7
	s_lshl_b32 s7, s15, 5
	s_and_b32 s22, s7, 0xfe0
	s_ashr_i32 s7, s6, 31
	s_lshl_b64 s[10:11], s[6:7], 12
	s_or_b32 s20, s10, s22
	v_or_b32_e32 v0, s20, v64
	v_mad_u64_u32 v[4:5], s[6:7], v0, s27, v[100:101]
	v_mad_i32_i24 v5, s11, v192, v5
	v_or_b32_e32 v110, s20, v66
	global_load_dwordx4 v[48:51], v[4:5], off offset:1024
	global_load_dwordx4 v[52:55], v[4:5], off offset:1056
	global_load_dwordx4 v[56:59], v[4:5], off offset:1088
	global_load_dwordx4 v[60:63], v[4:5], off offset:1120
	global_load_dwordx4 v[0:3], v[4:5], off offset:2048
	global_load_dwordx4 v[112:115], v[4:5], off offset:2080
	global_load_dwordx4 v[116:119], v[4:5], off offset:2112
	global_load_dwordx4 v[120:123], v[4:5], off offset:2144
	v_mad_u64_u32 v[4:5], s[6:7], v110, s27, v[102:103]
	v_mad_i32_i24 v5, s11, v192, v5
	v_add_co_u32_e32 v6, vcc, s26, v4
	s_movk_i32 s6, 0x3000
	s_nop 0
	v_addc_co_u32_e32 v7, vcc, 0, v5, vcc
	v_add_co_u32_e32 v8, vcc, s6, v4
	s_mov_b32 s6, 0x9000
	s_nop 0
	v_addc_co_u32_e32 v9, vcc, 0, v5, vcc
	v_add_co_u32_e32 v10, vcc, s87, v4
	s_mov_b32 s21, s11
	s_nop 0
	v_addc_co_u32_e32 v11, vcc, 0, v5, vcc
	v_add_co_u32_e32 v12, vcc, s6, v4
	s_mov_b32 s6, 0xa000
	s_nop 0
	v_addc_co_u32_e32 v13, vcc, 0, v5, vcc
	global_load_ushort v19, v[6:7], off offset:3584
	global_load_ushort v16, v[6:7], off offset:3648
	global_load_ushort v21, v[8:9], off
	global_load_ushort v17, v[8:9], off offset:64
	global_load_ushort v22, v[10:11], off offset:512
	global_load_ushort v18, v[10:11], off offset:576
	global_load_ushort v23, v[12:13], off offset:3072
	global_load_ushort v20, v[12:13], off offset:3136
	v_add_co_u32_e32 v6, vcc, s6, v4
	s_mov_b32 s6, 0xc000
	s_nop 0
	v_addc_co_u32_e32 v7, vcc, 0, v5, vcc
	v_add_co_u32_e32 v8, vcc, s6, v4
	s_mov_b32 s6, 0xd000
	s_nop 0
	v_addc_co_u32_e32 v9, vcc, 0, v5, vcc
	v_add_co_u32_e32 v10, vcc, s6, v4
	s_mov_b32 s6, 0x12000
	s_nop 0
	v_addc_co_u32_e32 v11, vcc, 0, v5, vcc
	v_add_co_u32_e32 v12, vcc, s6, v4
	s_mov_b32 s6, 0x13000
	s_nop 0
	v_addc_co_u32_e32 v13, vcc, 0, v5, vcc
	global_load_ushort v27, v[6:7], off offset:3584
	global_load_ushort v24, v[6:7], off offset:3648
	global_load_ushort v28, v[8:9], off
	global_load_ushort v25, v[8:9], off offset:64
	global_load_ushort v29, v[10:11], off offset:512
	global_load_ushort v26, v[10:11], off offset:576
	global_load_ushort v33, v[12:13], off offset:3072
	global_load_ushort v32, v[12:13], off offset:3136
	v_add_co_u32_e32 v6, vcc, s6, v4
	s_mov_b32 s6, 0x15000
	s_nop 0
	v_addc_co_u32_e32 v7, vcc, 0, v5, vcc
	v_add_co_u32_e32 v8, vcc, s6, v4
	s_mov_b32 s6, 0x16000
	s_nop 0
	v_addc_co_u32_e32 v9, vcc, 0, v5, vcc
	v_add_co_u32_e32 v10, vcc, s6, v4
	s_mov_b32 s6, 0x1b000
	s_nop 0
	v_addc_co_u32_e32 v11, vcc, 0, v5, vcc
	v_add_co_u32_e32 v12, vcc, s6, v4
	s_mov_b32 s6, 0x1c000
	s_nop 0
	v_addc_co_u32_e32 v13, vcc, 0, v5, vcc
	global_load_ushort v37, v[6:7], off offset:3584
	global_load_ushort v34, v[6:7], off offset:3648
	global_load_ushort v39, v[8:9], off
	global_load_ushort v35, v[8:9], off offset:64
	global_load_ushort v40, v[10:11], off offset:512
	global_load_ushort v36, v[10:11], off offset:576
	global_load_ushort v41, v[12:13], off offset:3072
	global_load_ushort v38, v[12:13], off offset:3136
	v_add_co_u32_e32 v6, vcc, s6, v4
	s_mov_b32 s6, 0x1e000
	s_nop 0
	v_addc_co_u32_e32 v7, vcc, 0, v5, vcc
	v_add_co_u32_e32 v8, vcc, s6, v4
	s_mov_b32 s6, 0x1f000
	s_nop 0
	v_addc_co_u32_e32 v9, vcc, 0, v5, vcc
	v_add_co_u32_e32 v10, vcc, s6, v4
	v_mov_b32_e32 v111, s11
	s_nop 0
	v_addc_co_u32_e32 v11, vcc, 0, v5, vcc
	global_load_ushort v31, v[4:5], off offset:3072
	global_load_ushort v30, v[4:5], off offset:3136
	global_load_ushort v45, v[6:7], off offset:3584
	global_load_ushort v42, v[6:7], off offset:3648
	global_load_ushort v46, v[8:9], off
	global_load_ushort v43, v[8:9], off offset:64
	global_load_ushort v47, v[10:11], off offset:512
	global_load_ushort v44, v[10:11], off offset:576
	s_nop 15
	s_nop 15
	s_waitcnt vmcnt(35)
	v_mfma_f32_32x32x16_bf16 v[0:15], v[0:3], v[48:51], 0
	s_waitcnt vmcnt(34)
	v_mfma_f32_32x32x16_bf16 v[0:15], v[112:115], v[52:55], v[0:15]
	s_waitcnt vmcnt(33)
	v_mfma_f32_32x32x16_bf16 v[0:15], v[116:119], v[56:59], v[0:15]
	s_waitcnt vmcnt(32)
	v_mfma_f32_32x32x16_bf16 v[0:15], v[120:123], v[60:63], v[0:15]
	s_nop 15
	s_nop 15
	s_nop 11
	v_mul_f32_e32 v0, 0x3e000000, v0
	v_mul_f32_e64 v79, |v0|, s28
	v_exp_f32_e32 v79, v79
	v_mul_f32_e32 v1, 0x3e000000, v1
	v_mul_f32_e64 v83, |v1|, s28
	v_exp_f32_e32 v83, v83
	v_add_f32_e32 v79, 1.0, v79
	v_cmp_gt_f32_e32 vcc, s29, v79
	v_mul_f32_e32 v2, 0x3e000000, v2
	v_mul_f32_e32 v3, 0x3e000000, v3
	v_cndmask_b32_e64 v81, 0, 32, vcc
	v_ldexp_f32 v79, v79, v81
	v_log_f32_e32 v79, v79
	v_cndmask_b32_e32 v85, 0, v193, vcc
	v_max_f32_e32 v81, 0, v0
	v_min_f32_e32 v0, 0, v0
	v_mul_f32_e32 v87, 0x3f317217, v79
	v_fma_f32 v87, v79, s30, -v87
	v_fmac_f32_e32 v87, 0x3377d1cf, v79
	v_fmac_f32_e32 v87, 0x3f317217, v79
	v_cmp_lt_f32_e64 vcc, |v79|, s31
	s_nop 1
	v_cndmask_b32_e32 v79, v79, v87, vcc
	v_sub_f32_e32 v79, v79, v85
	v_add_f32_e32 v81, v81, v79
	v_sub_f32_e32 v0, v0, v79
	v_add_f32_e32 v79, 1.0, v83
	v_cmp_gt_f32_e32 vcc, s29, v79
	v_cndmask_b32_e64 v81, 0, -v81, s[48:49]
	s_nop 0
	v_cndmask_b32_e64 v83, 0, 32, vcc
	v_ldexp_f32 v79, v79, v83
	v_log_f32_e32 v79, v79
	v_cndmask_b32_e64 v83, v194, v0, s[48:49]
	v_max_f32_e32 v0, 0, v1
	v_min_f32_e32 v1, 0, v1
	v_mul_f32_e32 v85, 0x3f317217, v79
	v_fma_f32 v85, v79, s30, -v85
	v_fmac_f32_e32 v85, 0x3377d1cf, v79
	v_fmac_f32_e32 v85, 0x3f317217, v79
	v_cmp_lt_f32_e64 s[6:7], |v79|, s31
	s_nop 1
	v_cndmask_b32_e64 v79, v79, v85, s[6:7]
	v_cndmask_b32_e32 v85, 0, v193, vcc
	v_sub_f32_e32 v79, v79, v85
	v_mul_f32_e64 v85, |v2|, s28
	v_exp_f32_e32 v85, v85
	v_add_f32_e32 v0, v0, v79
	v_sub_f32_e32 v1, v1, v79
	v_cndmask_b32_e64 v87, 0, -v0, s[50:51]
	v_add_f32_e32 v79, 1.0, v85
	v_cmp_gt_f32_e32 vcc, s29, v79
	v_max_f32_e32 v0, 0, v2
	v_min_f32_e32 v2, 0, v2
	v_cndmask_b32_e64 v85, 0, 32, vcc
	v_ldexp_f32 v79, v79, v85
	v_log_f32_e32 v79, v79
	v_cndmask_b32_e64 v85, v194, v1, s[50:51]
	v_mul_f32_e32 v1, 0x3f317217, v79
	v_fma_f32 v1, v79, s30, -v1
	v_fmac_f32_e32 v1, 0x3377d1cf, v79
	v_fmac_f32_e32 v1, 0x3f317217, v79
	v_cmp_lt_f32_e64 s[6:7], |v79|, s31
	s_nop 1
	v_cndmask_b32_e64 v1, v79, v1, s[6:7]
	v_cndmask_b32_e32 v79, 0, v193, vcc
	v_sub_f32_e32 v1, v1, v79
	v_mul_f32_e64 v79, |v3|, s28
	v_exp_f32_e32 v79, v79
	v_add_f32_e32 v0, v0, v1
	v_sub_f32_e32 v1, v2, v1
	v_cndmask_b32_e64 v89, 0, -v0, s[52:53]
	v_add_f32_e32 v2, 1.0, v79
	v_cmp_gt_f32_e32 vcc, s29, v2
	v_max_f32_e32 v0, 0, v3
	v_min_f32_e32 v3, 0, v3
	v_cndmask_b32_e64 v79, 0, 32, vcc
	v_ldexp_f32 v2, v2, v79
	v_log_f32_e32 v2, v2
	v_cndmask_b32_e64 v79, v194, v1, s[52:53]
	v_mul_f32_e32 v1, 0x3f317217, v2
	v_fma_f32 v1, v2, s30, -v1
	v_fmac_f32_e32 v1, 0x3377d1cf, v2
	v_fmac_f32_e32 v1, 0x3f317217, v2
	v_cmp_lt_f32_e64 s[6:7], |v2|, s31
	s_nop 1
	v_cndmask_b32_e64 v1, v2, v1, s[6:7]
	v_cndmask_b32_e32 v2, 0, v193, vcc
	v_sub_f32_e32 v1, v1, v2
	v_mul_f32_e32 v2, 0x3e000000, v4
	v_mul_f32_e64 v4, |v2|, s28
	v_exp_f32_e32 v4, v4
	v_add_f32_e32 v0, v0, v1
	v_sub_f32_e32 v1, v3, v1
	v_cndmask_b32_e64 v91, v194, v1, s[54:55]
	v_add_f32_e32 v3, 1.0, v4
	v_cmp_gt_f32_e32 vcc, s29, v3
	v_cndmask_b32_e64 v93, 0, -v0, s[54:55]
	v_max_f32_e32 v0, 0, v2
	v_cndmask_b32_e64 v4, 0, 32, vcc
	v_ldexp_f32 v3, v3, v4
	v_log_f32_e32 v3, v3
	v_min_f32_e32 v2, 0, v2
	v_mul_f32_e32 v1, 0x3f317217, v3
	v_fma_f32 v1, v3, s30, -v1
	v_fmac_f32_e32 v1, 0x3377d1cf, v3
	v_fmac_f32_e32 v1, 0x3f317217, v3
	v_cmp_lt_f32_e64 s[6:7], |v3|, s31
	s_nop 1
	v_cndmask_b32_e64 v1, v3, v1, s[6:7]
	v_cndmask_b32_e32 v3, 0, v193, vcc
	v_sub_f32_e32 v1, v1, v3
	v_mul_f32_e32 v3, 0x3e000000, v5
	v_mul_f32_e64 v4, |v3|, s28
	v_exp_f32_e32 v4, v4
	v_add_f32_e32 v0, v0, v1
	v_sub_f32_e32 v1, v2, v1
	v_cndmask_b32_e64 v95, v194, v1, s[56:57]
	v_add_f32_e32 v2, 1.0, v4
	v_cmp_gt_f32_e32 vcc, s29, v2
	v_cndmask_b32_e64 v5, 0, -v0, s[56:57]
	v_max_f32_e32 v0, 0, v3
	v_cndmask_b32_e64 v4, 0, 32, vcc
	v_ldexp_f32 v2, v2, v4
	v_log_f32_e32 v2, v2
	v_min_f32_e32 v3, 0, v3
	v_mul_f32_e32 v1, 0x3f317217, v2
	v_fma_f32 v1, v2, s30, -v1
	v_fmac_f32_e32 v1, 0x3377d1cf, v2
	v_fmac_f32_e32 v1, 0x3f317217, v2
	v_cmp_lt_f32_e64 s[6:7], |v2|, s31
	s_nop 1
	v_cndmask_b32_e64 v1, v2, v1, s[6:7]
	v_cndmask_b32_e32 v2, 0, v193, vcc
	v_sub_f32_e32 v1, v1, v2
	v_mul_f32_e32 v2, 0x3e000000, v6
	v_mul_f32_e64 v4, |v2|, s28
	v_exp_f32_e32 v4, v4
	v_add_f32_e32 v0, v0, v1
	v_sub_f32_e32 v1, v3, v1
	v_cndmask_b32_e64 v97, v194, v1, s[58:59]
	v_add_f32_e32 v3, 1.0, v4
	v_cmp_gt_f32_e32 vcc, s29, v3
	v_cndmask_b32_e64 v112, 0, -v0, s[58:59]
	v_max_f32_e32 v0, 0, v2
	v_cndmask_b32_e64 v4, 0, 32, vcc
	v_ldexp_f32 v3, v3, v4
	v_log_f32_e32 v3, v3
	v_min_f32_e32 v2, 0, v2
	v_mul_f32_e32 v1, 0x3f317217, v3
	v_fma_f32 v1, v3, s30, -v1
	v_fmac_f32_e32 v1, 0x3377d1cf, v3
	v_fmac_f32_e32 v1, 0x3f317217, v3
	v_cmp_lt_f32_e64 s[6:7], |v3|, s31
	s_nop 1
	v_cndmask_b32_e64 v1, v3, v1, s[6:7]
	v_cndmask_b32_e32 v3, 0, v193, vcc
	v_sub_f32_e32 v1, v1, v3
	v_mul_f32_e32 v3, 0x3e000000, v7
	v_mul_f32_e64 v4, |v3|, s28
	v_exp_f32_e32 v4, v4
	v_add_f32_e32 v0, v0, v1
	v_sub_f32_e32 v1, v2, v1
	v_cndmask_b32_e64 v113, v194, v1, s[60:61]
	v_add_f32_e32 v2, 1.0, v4
	v_cmp_gt_f32_e32 vcc, s29, v2
	v_cndmask_b32_e64 v114, 0, -v0, s[60:61]
	v_max_f32_e32 v0, 0, v3
	v_cndmask_b32_e64 v4, 0, 32, vcc
	v_ldexp_f32 v2, v2, v4
	v_log_f32_e32 v2, v2
	v_min_f32_e32 v3, 0, v3
	v_mul_f32_e32 v1, 0x3f317217, v2
	v_fma_f32 v1, v2, s30, -v1
	v_fmac_f32_e32 v1, 0x3377d1cf, v2
	v_fmac_f32_e32 v1, 0x3f317217, v2
	v_cmp_lt_f32_e64 s[6:7], |v2|, s31
	s_nop 1
	v_cndmask_b32_e64 v1, v2, v1, s[6:7]
	v_cndmask_b32_e32 v2, 0, v193, vcc
	v_sub_f32_e32 v1, v1, v2
	v_mul_f32_e32 v2, 0x3e000000, v8
	v_mul_f32_e64 v4, |v2|, s28
	v_exp_f32_e32 v4, v4
	v_add_f32_e32 v0, v0, v1
	v_sub_f32_e32 v1, v3, v1
	v_cndmask_b32_e64 v115, v194, v1, s[62:63]
	v_add_f32_e32 v3, 1.0, v4
	v_cmp_gt_f32_e32 vcc, s29, v3
	v_cndmask_b32_e64 v116, 0, -v0, s[62:63]
	v_max_f32_e32 v0, 0, v2
	v_cndmask_b32_e64 v4, 0, 32, vcc
	v_ldexp_f32 v3, v3, v4
	v_log_f32_e32 v3, v3
	v_min_f32_e32 v2, 0, v2
	v_mul_f32_e32 v1, 0x3f317217, v3
	v_fma_f32 v1, v3, s30, -v1
	v_fmac_f32_e32 v1, 0x3377d1cf, v3
	v_fmac_f32_e32 v1, 0x3f317217, v3
	v_cmp_lt_f32_e64 s[6:7], |v3|, s31
	s_nop 1
	v_cndmask_b32_e64 v1, v3, v1, s[6:7]
	v_cndmask_b32_e32 v3, 0, v193, vcc
	v_sub_f32_e32 v1, v1, v3
	v_mul_f32_e32 v3, 0x3e000000, v9
	v_mul_f32_e64 v4, |v3|, s28
	v_exp_f32_e32 v4, v4
	v_add_f32_e32 v0, v0, v1
	v_sub_f32_e32 v1, v2, v1
	v_cndmask_b32_e64 v117, v194, v1, s[64:65]
	v_add_f32_e32 v2, 1.0, v4
	v_cmp_gt_f32_e32 vcc, s29, v2
	s_nop 1
	v_cndmask_b32_e64 v4, 0, 32, vcc
	v_ldexp_f32 v2, v2, v4
	v_log_f32_e32 v4, v2
	v_cndmask_b32_e64 v2, 0, -v0, s[64:65]
	v_max_f32_e32 v0, 0, v3
	v_min_f32_e32 v3, 0, v3
	v_mul_f32_e32 v1, 0x3f317217, v4
	v_fma_f32 v1, v4, s30, -v1
	v_fmac_f32_e32 v1, 0x3377d1cf, v4
	v_fmac_f32_e32 v1, 0x3f317217, v4
	v_cmp_lt_f32_e64 s[6:7], |v4|, s31
	s_nop 1
	v_cndmask_b32_e64 v1, v4, v1, s[6:7]
	v_cndmask_b32_e32 v4, 0, v193, vcc
	v_sub_f32_e32 v1, v1, v4
	v_mul_f32_e32 v4, 0x3e000000, v10
	v_mul_f32_e64 v6, |v4|, s28
	v_exp_f32_e32 v6, v6
	v_add_f32_e32 v0, v0, v1
	v_sub_f32_e32 v1, v3, v1
	v_cndmask_b32_e64 v118, v194, v1, s[66:67]
	v_add_f32_e32 v3, 1.0, v6
	v_cmp_gt_f32_e32 vcc, s29, v3
	v_max_f32_e32 v1, 0, v4
	v_min_f32_e32 v4, 0, v4
	v_cndmask_b32_e64 v6, 0, 32, vcc
	v_ldexp_f32 v3, v3, v6
	v_log_f32_e32 v3, v3
	v_cndmask_b32_e64 v0, 0, -v0, s[66:67]
	v_mul_f32_e32 v6, 0x3f317217, v3
	v_fma_f32 v6, v3, s30, -v6
	v_fmac_f32_e32 v6, 0x3377d1cf, v3
	v_fmac_f32_e32 v6, 0x3f317217, v3
	v_cmp_lt_f32_e64 s[6:7], |v3|, s31
	s_nop 1
	v_cndmask_b32_e64 v3, v3, v6, s[6:7]
	v_cndmask_b32_e32 v6, 0, v193, vcc
	v_sub_f32_e32 v3, v3, v6
	v_mul_f32_e32 v6, 0x3e000000, v11
	v_mul_f32_e64 v7, |v6|, s28
	v_exp_f32_e32 v7, v7
	v_add_f32_e32 v1, v1, v3
	v_sub_f32_e32 v3, v4, v3
	v_cndmask_b32_e64 v119, v194, v3, s[68:69]
	v_add_f32_e32 v4, 1.0, v7
	v_cmp_gt_f32_e32 vcc, s29, v4
	v_cndmask_b32_e64 v122, 0, -v1, s[68:69]
	v_max_f32_e32 v1, 0, v6
	v_cndmask_b32_e64 v7, 0, 32, vcc
	v_ldexp_f32 v4, v4, v7
	v_log_f32_e32 v4, v4
	v_min_f32_e32 v6, 0, v6
	v_mul_f32_e32 v3, 0x3f317217, v4
	v_fma_f32 v3, v4, s30, -v3
	v_fmac_f32_e32 v3, 0x3377d1cf, v4
	v_fmac_f32_e32 v3, 0x3f317217, v4
	v_cmp_lt_f32_e64 s[6:7], |v4|, s31
	s_nop 1
	v_cndmask_b32_e64 v3, v4, v3, s[6:7]
	v_cndmask_b32_e32 v4, 0, v193, vcc
	v_sub_f32_e32 v3, v3, v4
	v_mul_f32_e32 v4, 0x3e000000, v12
	v_mul_f32_e64 v7, |v4|, s28
	v_exp_f32_e32 v7, v7
	v_add_f32_e32 v1, v1, v3
	v_sub_f32_e32 v3, v6, v3
	v_cndmask_b32_e64 v12, v194, v3, s[70:71]
	v_add_f32_e32 v6, 1.0, v7
	v_cmp_gt_f32_e32 vcc, s29, v6
	v_cndmask_b32_e64 v123, 0, -v1, s[70:71]
	v_max_f32_e32 v1, 0, v4
	v_cndmask_b32_e64 v7, 0, 32, vcc
	v_ldexp_f32 v6, v6, v7
	v_log_f32_e32 v6, v6
	v_min_f32_e32 v4, 0, v4
	v_mul_f32_e32 v3, 0x3f317217, v6
	v_fma_f32 v3, v6, s30, -v3
	v_fmac_f32_e32 v3, 0x3377d1cf, v6
	v_fmac_f32_e32 v3, 0x3f317217, v6
	v_cmp_lt_f32_e64 s[6:7], |v6|, s31
	s_nop 1
	v_cndmask_b32_e64 v3, v6, v3, s[6:7]
	v_cndmask_b32_e32 v6, 0, v193, vcc
	v_sub_f32_e32 v3, v3, v6
	v_mul_f32_e32 v6, 0x3e000000, v13
	v_mul_f32_e64 v7, |v6|, s28
	v_exp_f32_e32 v7, v7
	v_add_f32_e32 v1, v1, v3
	v_sub_f32_e32 v3, v4, v3
	v_cndmask_b32_e64 v13, v194, v3, s[72:73]
	v_add_f32_e32 v4, 1.0, v7
	v_cmp_gt_f32_e32 vcc, s29, v4
	v_max_f32_e32 v3, 0, v6
	v_min_f32_e32 v6, 0, v6
	v_cndmask_b32_e64 v7, 0, 32, vcc
	v_ldexp_f32 v4, v4, v7
	v_log_f32_e32 v4, v4
	v_cndmask_b32_e64 v1, 0, -v1, s[72:73]
	v_mul_f32_e32 v7, 0x3f317217, v4
	v_fma_f32 v7, v4, s30, -v7
	v_fmac_f32_e32 v7, 0x3377d1cf, v4
	v_fmac_f32_e32 v7, 0x3f317217, v4
	v_cmp_lt_f32_e64 s[6:7], |v4|, s31
	s_nop 1
	v_cndmask_b32_e64 v4, v4, v7, s[6:7]
	v_cndmask_b32_e32 v7, 0, v193, vcc
	v_sub_f32_e32 v4, v4, v7
	v_mul_f32_e32 v7, 0x3e000000, v14
	v_mul_f32_e64 v8, |v7|, s28
	v_exp_f32_e32 v8, v8
	v_add_f32_e32 v3, v3, v4
	v_sub_f32_e32 v4, v6, v4
	v_cndmask_b32_e64 v14, v194, v4, s[74:75]
	v_add_f32_e32 v6, 1.0, v8
	v_cmp_gt_f32_e32 vcc, s29, v6
	v_cndmask_b32_e64 v124, 0, -v3, s[74:75]
	v_max_f32_e32 v3, 0, v7
	v_cndmask_b32_e64 v8, 0, 32, vcc
	v_ldexp_f32 v6, v6, v8
	v_log_f32_e32 v6, v6
	v_min_f32_e32 v7, 0, v7
	v_mul_f32_e32 v4, 0x3f317217, v6
	v_fma_f32 v4, v6, s30, -v4
	v_fmac_f32_e32 v4, 0x3377d1cf, v6
	v_fmac_f32_e32 v4, 0x3f317217, v6
	v_cmp_lt_f32_e64 s[6:7], |v6|, s31
	s_nop 1
	v_cndmask_b32_e64 v4, v6, v4, s[6:7]
	v_cndmask_b32_e32 v6, 0, v193, vcc
	v_sub_f32_e32 v4, v4, v6
	v_mul_f32_e32 v6, 0x3e000000, v15
	v_mul_f32_e64 v8, |v6|, s28
	v_exp_f32_e32 v8, v8
	v_add_f32_e32 v3, v3, v4
	v_sub_f32_e32 v4, v7, v4
	v_cndmask_b32_e64 v15, v194, v4, s[76:77]
	v_add_f32_e32 v7, 1.0, v8
	v_cmp_gt_f32_e32 vcc, s29, v7
	v_cndmask_b32_e64 v125, 0, -v3, s[76:77]
	v_max_f32_e32 v3, 0, v6
	v_cndmask_b32_e64 v8, 0, 32, vcc
	v_ldexp_f32 v7, v7, v8
	v_log_f32_e32 v7, v7
	v_min_f32_e32 v6, 0, v6
	v_mul_f32_e32 v4, 0x3f317217, v7
	v_fma_f32 v4, v7, s30, -v4
	v_fmac_f32_e32 v4, 0x3377d1cf, v7
	v_fmac_f32_e32 v4, 0x3f317217, v7
	v_cmp_lt_f32_e64 s[6:7], |v7|, s31
	s_nop 1
	v_cndmask_b32_e64 v4, v7, v4, s[6:7]
	v_cndmask_b32_e32 v7, 0, v193, vcc
	v_sub_f32_e32 v4, v4, v7
	v_add_f32_e32 v3, v3, v4
	v_sub_f32_e32 v4, v6, v4
	v_cndmask_b32_e64 v126, v194, v4, s[78:79]
	v_cndmask_b32_e64 v127, 0, -v3, s[78:79]
	v_add_f32_e32 v3, v81, v87
	v_add_f32_e32 v4, v89, v93
	v_add_f32_e32 v4, v3, v4
	v_add_f32_e32 v3, v1, v124
	v_add_f32_e32 v1, v125, v127
	v_pk_add_f32 v[2:3], v[2:3], v[0:1]
	ds_bpermute_b32 v7, v184, v3
	v_add_f32_e32 v6, v122, v123
	v_add_f32_e32 v1, v5, v112
	v_add_f32_e32 v5, v114, v116
	ds_bpermute_b32 v8, v184, v4
	s_waitcnt lgkmcnt(0)
	v_pk_add_f32 v[2:3], v[2:3], v[6:7]
	ds_bpermute_b32 v144, v184, v2
	v_add_f32_e32 v6, v1, v5
	ds_bpermute_b32 v10, v184, v6
	v_add_f32_e32 v1, 0, v7
	v_cndmask_b32_e64 v1, 0, v1, s[42:43]
	s_waitcnt lgkmcnt(0)
	v_pk_add_f32 v[2:3], v[2:3], v[144:145]
	v_cndmask_b32_e64 v5, 0, v144, s[42:43]
	v_mov_b32_e32 v7, v2
	v_mov_b32_e32 v11, v3
	v_add_f32_e32 v81, v5, v3
	s_waitcnt lgkmcnt(0)
	v_cndmask_b32_e64 v5, 0, v10, s[42:43]
	v_pk_add_f32 v[2:3], v[6:7], v[10:11]
	v_cndmask_b32_e64 v7, 0, v8, s[42:43]
	v_add_f32_e32 v6, v5, v3
	v_mov_b32_e32 v5, v2
	v_mov_b32_e32 v9, v3
	v_pk_add_f32 v[120:121], v[4:5], v[8:9]
	v_add_f32_e32 v10, v12, v81
	v_add_f32_e32 v2, v7, v121
	v_add_f32_e32 v3, v91, v2
	v_add_f32_e32 v2, v93, v2
	v_mul_f32_e32 v10, 0x3fb8aa3b, v10
	v_add_f32_e32 v4, v79, v2
	v_exp_f32_e32 v79, v10
	v_add_f32_e32 v10, v123, v81
	v_add_f32_e32 v11, v119, v10
	v_add_f32_e32 v10, v122, v10
	v_add_f32_e32 v0, v0, v10
	v_add_f32_e32 v0, v117, v0
	v_add_f32_e32 v2, v89, v2
	v_add_f32_e32 v7, v115, v6
	v_add_f32_e32 v6, v116, v6
	v_mul_f32_e32 v0, 0x3fb8aa3b, v0
	v_add_f32_e32 v5, v85, v2
	v_add_f32_e32 v8, v113, v6
	v_add_f32_e32 v6, v114, v6
	v_exp_f32_e32 v85, v0
	v_add_f32_e32 v0, v126, v1
	v_add_f32_e32 v2, v87, v2
	v_add_f32_e32 v9, v97, v6
	v_add_f32_e32 v6, v112, v6
	v_mul_f32_e32 v0, 0x3fb8aa3b, v0
	v_add_f32_e32 v2, v83, v2
	v_add_f32_e32 v6, v95, v6
	v_exp_f32_e32 v87, v0
	v_add_f32_e32 v0, v127, v1
	v_mul_f32_e32 v3, 0x3fb8aa3b, v3
	v_mul_f32_e32 v4, 0x3fb8aa3b, v4
	v_mul_f32_e32 v5, 0x3fb8aa3b, v5
	v_mul_f32_e32 v2, 0x3fb8aa3b, v2
	v_mul_f32_e32 v7, 0x3fb8aa3b, v7
	v_mul_f32_e32 v8, 0x3fb8aa3b, v8
	v_mul_f32_e32 v9, 0x3fb8aa3b, v9
	v_mul_f32_e32 v6, 0x3fb8aa3b, v6
	v_add_f32_e32 v1, v15, v0
	v_exp_f32_e32 v3, v3
	v_exp_f32_e32 v4, v4
	v_exp_f32_e32 v5, v5
	v_exp_f32_e32 v2, v2
	v_exp_f32_e32 v7, v7
	v_exp_f32_e32 v8, v8
	v_exp_f32_e32 v9, v9
	v_exp_f32_e32 v6, v6
	v_mul_f32_e32 v1, 0x3fb8aa3b, v1
	v_add_f32_e32 v0, v125, v0
	v_mul_f32_e32 v11, 0x3fb8aa3b, v11
	v_exp_f32_e32 v89, v1
	v_add_f32_e32 v1, v14, v0
	v_add_f32_e32 v0, v124, v0
	v_exp_f32_e32 v81, v11
	v_add_f32_e32 v11, v118, v10
	v_add_f32_e32 v0, v13, v0
	v_mul_f32_e32 v11, 0x3fb8aa3b, v11
	v_mul_f32_e32 v1, 0x3fb8aa3b, v1
	v_mul_f32_e32 v0, 0x3fb8aa3b, v0
	v_exp_f32_e32 v83, v11
	v_exp_f32_e32 v91, v1
	v_exp_f32_e32 v93, v0
	s_nop 15
	s_nop 15
	v_cvt_pk_bf16_f32 v113, v4, v3
	v_cvt_pk_bf16_f32 v112, v2, v5
	v_cvt_pk_bf16_f32 v115, v8, v7
	v_cvt_pk_bf16_f32 v114, v6, v9
	s_waitcnt vmcnt(19)
	v_perm_b32 v3, v29, v28, s38
	v_perm_b32 v2, v27, v23, s38
	v_perm_b32 v1, v22, v21, s38
	s_waitcnt vmcnt(7)
	v_perm_b32 v0, v19, v31, s38
	v_perm_b32 v21, v26, v25, s38
	v_perm_b32 v20, v24, v20, s38
	v_perm_b32 v19, v18, v17, s38
	s_waitcnt vmcnt(6)
	v_perm_b32 v18, v16, v30, s38
	v_mfma_f32_32x32x16_bf16 v[0:15], v[112:115], v[0:3], 0
	s_waitcnt vmcnt(1)
	v_perm_b32 v119, v47, v46, s38
	v_perm_b32 v118, v45, v41, s38
	v_perm_b32 v117, v40, v39, s38
	v_perm_b32 v116, v37, v33, s38
	s_waitcnt vmcnt(0)
	v_perm_b32 v39, v44, v43, s38
	v_perm_b32 v38, v42, v38, s38
	v_perm_b32 v37, v36, v35, s38
	v_mfma_f32_32x32x16_bf16 v[16:31], v[112:115], v[18:21], 0
	v_cvt_pk_bf16_f32 v113, v81, v79
	v_cvt_pk_bf16_f32 v112, v85, v83
	v_cvt_pk_bf16_f32 v115, v89, v87
	v_cvt_pk_bf16_f32 v114, v93, v91
	v_perm_b32 v36, v34, v32, s38
	v_add_f32_e32 v95, v120, v121
	v_mfma_f32_32x32x16_bf16 v[0:15], v[112:115], v[116:119], v[0:15]
	v_mfma_f32_32x32x16_bf16 v[16:31], v[112:115], v[36:39], v[16:31]
	s_nop 15
	s_nop 15
	v_cmp_gt_f32_e32 vcc, s34, v95
	s_cmp_eq_u64 vcc, exec
	s_cselect_b64 s[6:7], -1, 0
	s_cmp_eq_u32 s22, 0
	s_cselect_b64 s[24:25], -1, 0
	s_or_b64 s[6:7], s[24:25], s[6:7]
	s_and_b64 vcc, exec, s[6:7]
	s_cbranch_vccnz .LBB0_256
	s_and_b32 s6, s14, 0xfe0
	s_sub_i32 s6, s6, 32
	s_add_u32 s6, s6, s10
	s_addc_u32 s7, 0, s11
	v_lshl_add_u64 v[32:33], s[6:7], 0, v[66:67]
	v_mad_u64_u32 v[112:113], s[10:11], v32, s27, v[106:107]
	v_mad_i32_i24 v113, v33, s27, v113
	v_lshl_add_u64 v[32:33], s[6:7], 0, v[64:65]
	v_mad_u64_u32 v[114:115], s[6:7], v32, s27, v[108:109]
	s_mov_b32 s24, 0xfffdc000
	v_mad_i32_i24 v115, v33, s27, v115
	s_mov_b32 s25, -1
.LBB0_255:
	v_lshl_add_u64 v[36:37], v[114:115], 0, v[98:99]
	global_load_dwordx4 v[32:35], v[36:37], off offset:-64
	global_load_dwordx4 v[116:119], v[36:37], off offset:-32
	global_load_dwordx4 v[120:123], v[36:37], off
	global_load_dwordx4 v[124:127], v[36:37], off offset:32
	v_lshl_add_u64 v[36:37], v[112:113], 0, v[98:99]
	v_add_co_u32_e32 v38, vcc, 0x8640000, v36
	s_sub_i32 s10, s22, 32
	s_nop 0
	v_addc_co_u32_e32 v39, vcc, 0, v37, vcc
	v_add_co_u32_e32 v40, vcc, 0x8641000, v36
	s_nop 1
	v_addc_co_u32_e32 v41, vcc, 0, v37, vcc
	v_add_co_u32_e32 v42, vcc, 0x8643000, v36
	s_nop 1
	v_addc_co_u32_e32 v43, vcc, 0, v37, vcc
	v_add_co_u32_e32 v44, vcc, 0x8644000, v36
	s_nop 1
	v_addc_co_u32_e32 v45, vcc, 0, v37, vcc
	global_load_ushort v85, v[38:39], off offset:3072
	global_load_ushort v79, v[38:39], off offset:3136
	global_load_ushort v89, v[40:41], off offset:3584
	global_load_ushort v81, v[40:41], off offset:3648
	global_load_ushort v91, v[42:43], off
	global_load_ushort v83, v[42:43], off offset:64
	global_load_ushort v93, v[44:45], off offset:512
	global_load_ushort v87, v[44:45], off offset:576
	v_add_co_u32_e32 v38, vcc, 0x8649000, v36
	s_nop 1
	v_addc_co_u32_e32 v39, vcc, 0, v37, vcc
	v_add_co_u32_e32 v40, vcc, 0x864a000, v36
	s_nop 1
	v_addc_co_u32_e32 v41, vcc, 0, v37, vcc
	v_add_co_u32_e32 v42, vcc, 0x864c000, v36
	s_nop 1
	v_addc_co_u32_e32 v43, vcc, 0, v37, vcc
	v_add_co_u32_e32 v44, vcc, 0x864d000, v36
	s_nop 1
	v_addc_co_u32_e32 v45, vcc, 0, v37, vcc
	global_load_ushort v139, v[38:39], off offset:3072
	global_load_ushort v97, v[38:39], off offset:3136
	global_load_ushort v142, v[40:41], off offset:3584
	global_load_ushort v136, v[40:41], off offset:3648
	global_load_ushort v144, v[42:43], off
	global_load_ushort v137, v[42:43], off offset:64
	global_load_ushort v154, v[44:45], off offset:512
	global_load_ushort v140, v[44:45], off offset:576
	v_add_co_u32_e32 v38, vcc, 0x8652000, v36
	s_nop 1
	v_addc_co_u32_e32 v39, vcc, 0, v37, vcc
	v_add_co_u32_e32 v40, vcc, 0x8653000, v36
	s_nop 1
	v_addc_co_u32_e32 v41, vcc, 0, v37, vcc
	v_add_co_u32_e32 v42, vcc, 0x8655000, v36
	s_nop 1
	v_addc_co_u32_e32 v43, vcc, 0, v37, vcc
	v_add_co_u32_e32 v44, vcc, 0x8656000, v36
	s_nop 1
	v_addc_co_u32_e32 v45, vcc, 0, v37, vcc
	global_load_ushort v152, v[38:39], off offset:3072
	global_load_ushort v138, v[38:39], off offset:3136
	global_load_ushort v155, v[40:41], off offset:3584
	global_load_ushort v141, v[40:41], off offset:3648
	global_load_ushort v156, v[42:43], off
	global_load_ushort v143, v[42:43], off offset:64
	global_load_ushort v157, v[44:45], off offset:512
	global_load_ushort v153, v[44:45], off offset:576
	v_add_co_u32_e32 v38, vcc, 0x865b000, v36
	s_nop 1
	v_addc_co_u32_e32 v39, vcc, 0, v37, vcc
	v_add_co_u32_e32 v40, vcc, 0x865c000, v36
	s_nop 1
	v_addc_co_u32_e32 v41, vcc, 0, v37, vcc
	v_add_co_u32_e32 v42, vcc, 0x865e000, v36
	s_nop 1
	v_addc_co_u32_e32 v43, vcc, 0, v37, vcc
	v_add_co_u32_e32 v36, vcc, 0x865f000, v36
	s_nop 1
	v_addc_co_u32_e32 v37, vcc, 0, v37, vcc
	global_load_ushort v161, v[38:39], off offset:3072
	global_load_ushort v158, v[38:39], off offset:3136
	global_load_ushort v163, v[40:41], off offset:3584
	global_load_ushort v159, v[40:41], off offset:3648
	global_load_ushort v164, v[42:43], off
	global_load_ushort v160, v[42:43], off offset:64
	global_load_ushort v165, v[36:37], off offset:512
	global_load_ushort v162, v[36:37], off offset:576
	s_nop 15
	s_nop 15
	s_waitcnt vmcnt(35)
	v_mfma_f32_32x32x16_bf16 v[32:47], v[32:35], v[48:51], 0
	s_waitcnt vmcnt(34)
	v_mfma_f32_32x32x16_bf16 v[32:47], v[116:119], v[52:55], v[32:47]
	s_waitcnt vmcnt(33)
	v_mfma_f32_32x32x16_bf16 v[32:47], v[120:123], v[56:59], v[32:47]
	s_waitcnt vmcnt(32)
	v_mfma_f32_32x32x16_bf16 v[32:47], v[124:127], v[60:63], v[32:47]
	s_nop 15
	s_nop 15
	s_nop 11
	v_mul_f32_e32 v117, 0x3e000000, v32
	v_mul_f32_e64 v32, |v117|, s28
	v_exp_f32_e32 v32, v32
	v_mul_f32_e32 v33, 0x3e000000, v33
	v_mul_f32_e32 v121, 0x3e000000, v34
	v_mul_f32_e64 v34, |v121|, s28
	v_add_f32_e32 v32, 1.0, v32
	v_cmp_gt_f32_e32 vcc, s29, v32
	v_exp_f32_e32 v34, v34
	v_max_f32_e32 v122, 0, v117
	v_cndmask_b32_e64 v116, 0, 32, vcc
	v_ldexp_f32 v32, v32, v116
	v_log_f32_e32 v32, v32
	v_mul_f32_e64 v116, |v33|, s28
	v_exp_f32_e32 v116, v116
	v_cndmask_b32_e32 v118, 0, v193, vcc
	v_mul_f32_e32 v119, 0x3f317217, v32
	v_fma_f32 v119, v32, s30, -v119
	v_fmac_f32_e32 v119, 0x3377d1cf, v32
	v_fmac_f32_e32 v119, 0x3f317217, v32
	v_cmp_lt_f32_e64 vcc, |v32|, s31
	v_add_f32_e32 v116, 1.0, v116
	v_add_f32_e32 v34, 1.0, v34
	v_cndmask_b32_e32 v32, v32, v119, vcc
	v_cmp_gt_f32_e32 vcc, s29, v116
	v_sub_f32_e32 v32, v32, v118
	v_max_f32_e32 v124, 0, v33
	v_cndmask_b32_e64 v119, 0, 32, vcc
	v_ldexp_f32 v116, v116, v119
	v_log_f32_e32 v119, v116
	v_min_f32_e32 v116, 0, v117
	v_cndmask_b32_e32 v118, 0, v193, vcc
	v_cmp_gt_f32_e32 vcc, s29, v34
	v_mul_f32_e32 v117, 0x3f317217, v119
	v_fma_f32 v117, v119, s30, -v117
	v_fmac_f32_e32 v117, 0x3377d1cf, v119
	v_fmac_f32_e32 v117, 0x3f317217, v119
	v_cmp_lt_f32_e64 s[6:7], |v119|, s31
	v_mul_f32_e32 v36, 0x3e000000, v36
	v_max_f32_e32 v123, 0, v121
	v_cndmask_b32_e64 v117, v119, v117, s[6:7]
	v_cndmask_b32_e64 v119, 0, 32, vcc
	v_ldexp_f32 v34, v34, v119
	v_log_f32_e32 v119, v34
	v_sub_f32_e32 v34, v117, v118
	v_mul_f32_e32 v117, 0x3e000000, v35
	v_mul_f32_e64 v35, |v117|, s28
	v_exp_f32_e32 v35, v35
	v_min_f32_e32 v118, 0, v33
	v_mul_f32_e32 v33, 0x3f317217, v119
	v_fma_f32 v33, v119, s30, -v33
	v_fmac_f32_e32 v33, 0x3377d1cf, v119
	v_fmac_f32_e32 v33, 0x3f317217, v119
	v_cmp_lt_f32_e64 s[6:7], |v119|, s31
	v_add_f32_e32 v35, 1.0, v35
	v_max_f32_e32 v125, 0, v117
	v_cndmask_b32_e64 v33, v119, v33, s[6:7]
	v_cndmask_b32_e32 v119, 0, v193, vcc
	v_cmp_gt_f32_e32 vcc, s29, v35
	v_sub_f32_e32 v33, v33, v119
	v_mul_f32_e32 v37, 0x3e000000, v37
	v_cndmask_b32_e64 v120, 0, 32, vcc
	v_ldexp_f32 v35, v35, v120
	v_log_f32_e32 v35, v35
	v_min_f32_e32 v120, 0, v121
	v_mul_f32_e64 v121, |v36|, s28
	v_exp_f32_e32 v121, v121
	v_mul_f32_e32 v119, 0x3f317217, v35
	v_fma_f32 v119, v35, s30, -v119
	v_fmac_f32_e32 v119, 0x3377d1cf, v35
	v_fmac_f32_e32 v119, 0x3f317217, v35
	v_cmp_lt_f32_e64 s[6:7], |v35|, s31
	v_mul_f32_e32 v39, 0x3e000000, v39
	v_mul_f32_e32 v41, 0x3e000000, v41
	v_cndmask_b32_e64 v35, v35, v119, s[6:7]
	v_cndmask_b32_e32 v119, 0, v193, vcc
	v_sub_f32_e32 v35, v35, v119
	v_add_f32_e32 v119, 1.0, v121
	v_cmp_gt_f32_e32 vcc, s29, v119
	v_min_f32_e32 v132, 0, v41
	v_max_f32_e32 v168, 0, v41
	v_cndmask_b32_e64 v121, 0, 32, vcc
	v_ldexp_f32 v119, v119, v121
	v_log_f32_e32 v119, v119
	v_min_f32_e32 v121, 0, v117
	v_sub_f32_e32 v131, v121, v35
	v_cndmask_b32_e32 v121, 0, v193, vcc
	v_mul_f32_e32 v117, 0x3f317217, v119
	v_fma_f32 v117, v119, s30, -v117
	v_fmac_f32_e32 v117, 0x3377d1cf, v119
	v_fmac_f32_e32 v117, 0x3f317217, v119
	v_cmp_lt_f32_e64 s[6:7], |v119|, s31
	v_mul_f32_e32 v45, 0x3e000000, v45
	v_min_f32_e32 v176, 0, v45
	v_cndmask_b32_e64 v117, v119, v117, s[6:7]
	v_mul_f32_e64 v119, |v37|, s28
	v_exp_f32_e32 v119, v119
	v_sub_f32_e32 v117, v117, v121
	v_min_f32_e32 v121, 0, v36
	v_sub_f32_e32 v133, v121, v117
	v_add_f32_e32 v119, 1.0, v119
	v_cmp_gt_f32_e32 vcc, s29, v119
	v_mul_f32_e32 v121, 0x3e000000, v38
	v_mul_f32_e64 v38, |v121|, s28
	v_cndmask_b32_e64 v126, 0, 32, vcc
	v_ldexp_f32 v119, v119, v126
	v_log_f32_e32 v119, v119
	v_max_f32_e32 v36, 0, v36
	v_exp_f32_e32 v38, v38
	v_add_f32_e32 v117, v36, v117
	v_mul_f32_e32 v36, 0x3f317217, v119
	v_fma_f32 v36, v119, s30, -v36
	v_fmac_f32_e32 v36, 0x3377d1cf, v119
	v_fmac_f32_e32 v36, 0x3f317217, v119
	v_cmp_lt_f32_e64 s[6:7], |v119|, s31
	v_add_f32_e32 v38, 1.0, v38
	v_mul_f32_e64 v126, |v39|, s28
	v_cndmask_b32_e64 v36, v119, v36, s[6:7]
	v_cndmask_b32_e32 v119, 0, v193, vcc
	v_cmp_gt_f32_e32 vcc, s29, v38
	v_sub_f32_e32 v36, v36, v119
	v_exp_f32_e32 v127, v126
	v_cndmask_b32_e64 v119, 0, 32, vcc
	v_ldexp_f32 v38, v38, v119
	v_log_f32_e32 v119, v38
	v_min_f32_e32 v38, 0, v37
	v_max_f32_e32 v37, 0, v37
	v_add_f32_e32 v171, v37, v36
	v_mul_f32_e32 v37, 0x3f317217, v119
	v_fma_f32 v37, v119, s30, -v37
	v_fmac_f32_e32 v37, 0x3377d1cf, v119
	v_fmac_f32_e32 v37, 0x3f317217, v119
	v_cmp_lt_f32_e64 s[6:7], |v119|, s31
	v_min_f32_e32 v128, 0, v121
	v_max_f32_e32 v178, 0, v45
	v_cndmask_b32_e64 v37, v119, v37, s[6:7]
	v_cndmask_b32_e32 v119, 0, v193, vcc
	v_sub_f32_e32 v126, v37, v119
	v_add_f32_e32 v37, 1.0, v127
	v_cmp_gt_f32_e32 vcc, s29, v37
	v_pk_add_f32 v[124:125], v[124:125], v[34:35]
	v_sub_f32_e64 v206, -v171, v117
	v_cndmask_b32_e64 v119, 0, 32, vcc
	v_ldexp_f32 v37, v37, v119
	v_log_f32_e32 v119, v37
	v_max_f32_e32 v37, 0, v121
	v_cndmask_b32_e32 v127, 0, v193, vcc
	v_add_f32_e32 v37, v37, v126
	v_mul_f32_e32 v121, 0x3f317217, v119
	v_fma_f32 v121, v119, s30, -v121
	v_fmac_f32_e32 v121, 0x3377d1cf, v119
	v_fmac_f32_e32 v121, 0x3f317217, v119
	v_cmp_lt_f32_e64 s[6:7], |v119|, s31
	v_pk_add_f32 v[122:123], v[122:123], v[32:33]
	s_nop 0
	v_cndmask_b32_e64 v119, v119, v121, s[6:7]
	v_mul_f32_e32 v121, 0x3e000000, v40
	v_mul_f32_e64 v40, |v121|, s28
	v_exp_f32_e32 v40, v40
	v_sub_f32_e32 v119, v119, v127
	v_min_f32_e32 v127, 0, v39
	v_max_f32_e32 v39, 0, v39
	v_add_f32_e32 v40, 1.0, v40
	v_cmp_gt_f32_e32 vcc, s29, v40
	v_sub_f32_e32 v174, v127, v119
	v_add_f32_e32 v127, v39, v119
	v_cndmask_b32_e64 v129, 0, 32, vcc
	v_ldexp_f32 v40, v40, v129
	v_log_f32_e32 v40, v40
	v_mul_f32_e64 v119, |v41|, s28
	v_exp_f32_e32 v119, v119
	v_min_f32_e32 v130, 0, v121
	v_mul_f32_e32 v39, 0x3f317217, v40
	v_fma_f32 v39, v40, s30, -v39
	v_fmac_f32_e32 v39, 0x3377d1cf, v40
	v_fmac_f32_e32 v39, 0x3f317217, v40
	v_cmp_lt_f32_e64 s[6:7], |v40|, s31
	v_add_f32_e32 v119, 1.0, v119
	v_max_f32_e32 v166, 0, v121
	v_cndmask_b32_e64 v39, v40, v39, s[6:7]
	v_cndmask_b32_e32 v40, 0, v193, vcc
	v_cmp_gt_f32_e32 vcc, s29, v119
	v_mul_f32_e32 v121, 0x3e000000, v42
	v_mul_f32_e64 v42, |v121|, s28
	v_cndmask_b32_e64 v129, 0, 32, vcc
	v_ldexp_f32 v119, v119, v129
	v_log_f32_e32 v119, v119
	v_exp_f32_e32 v42, v42
	v_sub_f32_e32 v40, v39, v40
	v_min_f32_e32 v134, 0, v121
	v_mul_f32_e32 v39, 0x3f317217, v119
	v_fma_f32 v39, v119, s30, -v39
	v_fmac_f32_e32 v39, 0x3377d1cf, v119
	v_fmac_f32_e32 v39, 0x3f317217, v119
	v_cmp_lt_f32_e64 s[6:7], |v119|, s31
	v_add_f32_e32 v42, 1.0, v42
	v_max_f32_e32 v167, 0, v121
	v_cndmask_b32_e64 v39, v119, v39, s[6:7]
	v_cndmask_b32_e32 v119, 0, v193, vcc
	v_cmp_gt_f32_e32 vcc, s29, v42
	v_mul_f32_e32 v121, 0x3e000000, v44
	v_min_f32_e32 v170, 0, v121
	v_cndmask_b32_e64 v129, 0, 32, vcc
	v_ldexp_f32 v42, v42, v129
	v_log_f32_e32 v129, v42
	v_sub_f32_e32 v42, v39, v119
	v_mul_f32_e32 v119, 0x3e000000, v43
	v_mul_f32_e64 v41, |v119|, s28
	v_exp_f32_e32 v41, v41
	v_mul_f32_e32 v39, 0x3f317217, v129
	v_fma_f32 v39, v129, s30, -v39
	v_fmac_f32_e32 v39, 0x3377d1cf, v129
	v_add_f32_e32 v41, 1.0, v41
	v_fmac_f32_e32 v39, 0x3f317217, v129
	v_cmp_lt_f32_e64 s[6:7], |v129|, s31
	v_cndmask_b32_e32 v43, 0, v193, vcc
	v_cmp_gt_f32_e32 vcc, s29, v41
	v_cndmask_b32_e64 v39, v129, v39, s[6:7]
	v_max_f32_e32 v169, 0, v119
	v_cndmask_b32_e64 v129, 0, 32, vcc
	v_ldexp_f32 v41, v41, v129
	v_log_f32_e32 v129, v41
	v_sub_f32_e32 v41, v39, v43
	v_mul_f32_e64 v43, |v121|, s28
	v_exp_f32_e32 v44, v43
	v_mul_f32_e32 v39, 0x3f317217, v129
	v_fma_f32 v39, v129, s30, -v39
	v_fmac_f32_e32 v39, 0x3377d1cf, v129
	v_fmac_f32_e32 v39, 0x3f317217, v129
	v_cmp_lt_f32_e64 s[6:7], |v129|, s31
	v_cndmask_b32_e32 v43, 0, v193, vcc
	v_max_f32_e32 v172, 0, v121
	v_cndmask_b32_e64 v39, v129, v39, s[6:7]
	v_sub_f32_e32 v43, v39, v43
	v_add_f32_e32 v39, 1.0, v44
	v_cmp_gt_f32_e32 vcc, s29, v39
	v_mul_f32_e32 v121, 0x3e000000, v46
	v_mul_f32_e64 v46, |v121|, s28
	v_cndmask_b32_e64 v44, 0, 32, vcc
	v_ldexp_f32 v39, v39, v44
	v_log_f32_e32 v39, v39
	v_min_f32_e32 v44, 0, v119
	v_mul_f32_e64 v119, |v45|, s28
	v_exp_f32_e32 v119, v119
	v_sub_f32_e32 v177, v44, v43
	v_mul_f32_e32 v44, 0x3f317217, v39
	v_fma_f32 v44, v39, s30, -v44
	v_fmac_f32_e32 v44, 0x3377d1cf, v39
	v_fmac_f32_e32 v44, 0x3f317217, v39
	v_cmp_lt_f32_e64 s[6:7], |v39|, s31
	v_add_f32_e32 v119, 1.0, v119
	v_exp_f32_e32 v46, v46
	v_cndmask_b32_e64 v39, v39, v44, s[6:7]
	v_cndmask_b32_e32 v44, 0, v193, vcc
	v_cmp_gt_f32_e32 vcc, s29, v119
	v_sub_f32_e32 v44, v39, v44
	v_add_f32_e32 v46, 1.0, v46
	v_cndmask_b32_e64 v129, 0, 32, vcc
	v_ldexp_f32 v119, v119, v129
	v_log_f32_e32 v119, v119
	v_pk_add_f32 v[166:167], v[166:167], v[40:41]
	v_pk_add_f32 v[168:169], v[168:169], v[42:43]
	v_max_f32_e32 v173, 0, v121
	v_mul_f32_e32 v39, 0x3f317217, v119
	v_fma_f32 v39, v119, s30, -v39
	v_fmac_f32_e32 v39, 0x3377d1cf, v119
	v_fmac_f32_e32 v39, 0x3f317217, v119
	v_cmp_lt_f32_e64 s[6:7], |v119|, s31
	v_pk_add_f32 v[208:209], v[168:169], v[166:167] neg_lo:[1,1] neg_hi:[1,1]
	v_sub_f32_e64 v210, -v127, v37
	v_cndmask_b32_e64 v39, v119, v39, s[6:7]
	v_cndmask_b32_e32 v119, 0, v193, vcc
	v_cmp_gt_f32_e32 vcc, s29, v46
	v_pk_add_f32 v[208:209], v[208:209], v[208:209] op_sel:[0,1] op_sel_hi:[1,0]
	ds_bpermute_b32 v211, v184, v208
	v_cndmask_b32_e64 v129, 0, 32, vcc
	v_ldexp_f32 v46, v46, v129
	v_log_f32_e32 v129, v46
	v_sub_f32_e32 v46, v39, v119
	v_mul_f32_e32 v119, 0x3e000000, v47
	v_mul_f32_e64 v45, |v119|, s28
	v_exp_f32_e32 v45, v45
	v_mul_f32_e32 v39, 0x3f317217, v129
	v_fma_f32 v39, v129, s30, -v39
	v_fmac_f32_e32 v39, 0x3377d1cf, v129
	v_add_f32_e32 v45, 1.0, v45
	v_fmac_f32_e32 v39, 0x3f317217, v129
	v_cmp_lt_f32_e64 s[6:7], |v129|, s31
	v_cndmask_b32_e32 v47, 0, v193, vcc
	v_cmp_gt_f32_e32 vcc, s29, v45
	v_cndmask_b32_e64 v39, v129, v39, s[6:7]
	v_max_f32_e32 v179, 0, v119
	v_cndmask_b32_e64 v129, 0, 32, vcc
	v_ldexp_f32 v45, v45, v129
	v_log_f32_e32 v129, v45
	v_sub_f32_e32 v45, v39, v47
	v_cndmask_b32_e32 v47, 0, v193, vcc
	v_pk_add_f32 v[172:173], v[172:173], v[44:45]
	v_mul_f32_e32 v39, 0x3f317217, v129
	v_fma_f32 v39, v129, s30, -v39
	v_fmac_f32_e32 v39, 0x3377d1cf, v129
	v_fmac_f32_e32 v39, 0x3f317217, v129
	v_cmp_lt_f32_e64 s[6:7], |v129|, s31
	v_mov_b32_e32 v207, v208
	s_waitcnt lgkmcnt(0)
	v_pk_add_f32 v[206:207], v[206:207], v[210:211]
	v_cndmask_b32_e64 v39, v129, v39, s[6:7]
	v_sub_f32_e32 v47, v39, v47
	v_pk_add_f32 v[178:179], v[178:179], v[46:47]
	v_min_f32_e32 v39, 0, v119
	v_pk_add_f32 v[212:213], v[178:179], v[172:173] neg_lo:[1,1] neg_hi:[1,1]
	v_sub_f32_e32 v190, v39, v47
	v_add_f32_e32 v35, v212, v213
	ds_bpermute_b32 v39, v184, v35
	ds_bpermute_b32 v208, v184, v206
	v_pk_add_f32 v[182:183], v[124:125], v[122:123] neg_lo:[1,1] neg_hi:[1,1]
	v_min_f32_e32 v180, 0, v121
	v_mov_b32_e32 v212, v182
	s_waitcnt lgkmcnt(0)
	v_add_f32_e32 v35, v35, v39
	v_add_f32_e32 v209, v95, v35
	s_waitcnt lgkmcnt(0)
	v_pk_add_f32 v[206:207], v[206:207], v[208:209]
	v_cndmask_b32_e64 v43, 0, v39, s[42:43]
	v_mov_b32_e32 v213, v206
	v_mov_b32_e32 v206, v183
	v_pk_add_f32 v[182:183], v[212:213], v[206:207]
	v_add_f32_e32 v181, v95, v43
	ds_bpermute_b32 v95, v184, v182
	v_cndmask_b32_e64 v35, 0, v211, s[42:43]
	v_add_f32_e32 v135, v35, v209
	v_cndmask_b32_e64 v35, 0, v208, s[42:43]
	v_add_f32_e32 v129, v35, v207
	s_waitcnt lgkmcnt(0)
	v_cndmask_b32_e64 v35, 0, v95, s[42:43]
	v_add_f32_e32 v121, v35, v183
	v_add_f32_e32 v35, v131, v121
	v_mov_b32_e32 v206, v33
	v_mov_b32_e32 v207, v125
	v_mul_f32_e32 v35, 0x3fb8aa3b, v35
	v_pk_add_f32 v[120:121], v[120:121], v[206:207] neg_lo:[0,1] neg_hi:[0,1]
	v_exp_f32_e32 v122, v35
	v_add_f32_e32 v33, v120, v121
	v_mov_b32_e32 v119, v121
	v_mov_b32_e32 v35, v123
	v_mul_f32_e32 v33, 0x3fb8aa3b, v33
	v_pk_add_f32 v[34:35], v[118:119], v[34:35] neg_lo:[0,1] neg_hi:[0,1]
	v_exp_f32_e32 v120, v33
	v_add_f32_e32 v33, v34, v35
	v_mul_f32_e32 v33, 0x3fb8aa3b, v33
	v_exp_f32_e32 v34, v33
	v_mov_b32_e32 v117, v35
	v_mov_b32_e32 v33, v124
	v_pk_add_f32 v[32:33], v[116:117], v[32:33] neg_lo:[0,1] neg_hi:[0,1]
	v_mov_b32_e32 v43, v167
	v_add_f32_e32 v32, v32, v33
	v_mul_f32_e32 v32, 0x3fb8aa3b, v32
	v_exp_f32_e32 v35, v32
	v_add_f32_e32 v32, v174, v129
	v_mul_f32_e32 v32, 0x3fb8aa3b, v32
	v_exp_f32_e32 v116, v32
	v_pk_add_f32 v[32:33], v[128:129], v[126:127] neg_lo:[0,1] neg_hi:[0,1]
	v_mov_b32_e32 v47, v173
	v_add_f32_e32 v32, v32, v33
	v_mul_f32_e32 v32, 0x3fb8aa3b, v32
	v_mov_b32_e32 v39, v33
	v_exp_f32_e32 v117, v32
	v_pk_add_f32 v[32:33], v[38:39], v[36:37] neg_lo:[0,1] neg_hi:[0,1]
	s_nop 0
	v_add_f32_e32 v32, v32, v33
	v_mul_f32_e32 v32, 0x3fb8aa3b, v32
	v_exp_f32_e32 v36, v32
	v_sub_f32_e32 v32, v33, v171
	v_add_f32_e32 v32, v133, v32
	v_mul_f32_e32 v32, 0x3fb8aa3b, v32
	v_exp_f32_e32 v37, v32
	v_add_f32_e32 v32, v177, v135
	v_mul_f32_e32 v32, 0x3fb8aa3b, v32
	v_exp_f32_e32 v118, v32
	v_mov_b32_e32 v32, v41
	v_mov_b32_e32 v33, v169
	v_pk_add_f32 v[32:33], v[134:135], v[32:33] neg_lo:[0,1] neg_hi:[0,1]
	v_mov_b32_e32 v41, v168
	v_add_f32_e32 v32, v32, v33
	v_mul_f32_e32 v32, 0x3fb8aa3b, v32
	v_mov_b32_e32 v133, v33
	v_exp_f32_e32 v119, v32
	v_pk_add_f32 v[32:33], v[132:133], v[42:43] neg_lo:[0,1] neg_hi:[0,1]
	s_nop 0
	v_add_f32_e32 v32, v32, v33
	v_mul_f32_e32 v32, 0x3fb8aa3b, v32
	v_mov_b32_e32 v131, v33
	v_exp_f32_e32 v42, v32
	v_pk_add_f32 v[32:33], v[130:131], v[40:41] neg_lo:[0,1] neg_hi:[0,1]
	s_nop 0
	v_add_f32_e32 v32, v32, v33
	v_mul_f32_e32 v32, 0x3fb8aa3b, v32
	v_exp_f32_e32 v40, v32
	v_add_f32_e32 v32, v190, v181
	v_mul_f32_e32 v32, 0x3fb8aa3b, v32
	v_exp_f32_e32 v41, v32
	v_mov_b32_e32 v32, v45
	v_mov_b32_e32 v33, v179
	v_pk_add_f32 v[32:33], v[180:181], v[32:33] neg_lo:[0,1] neg_hi:[0,1]
	v_mov_b32_e32 v45, v178
	v_add_f32_e32 v32, v32, v33
	v_mul_f32_e32 v32, 0x3fb8aa3b, v32
	v_mov_b32_e32 v177, v33
	v_exp_f32_e32 v43, v32
	v_pk_add_f32 v[32:33], v[176:177], v[46:47] neg_lo:[0,1] neg_hi:[0,1]
	s_nop 0
	v_add_f32_e32 v32, v32, v33
	v_mul_f32_e32 v32, 0x3fb8aa3b, v32
	v_mov_b32_e32 v171, v33
	v_exp_f32_e32 v46, v32
	v_pk_add_f32 v[32:33], v[170:171], v[44:45] neg_lo:[0,1] neg_hi:[0,1]
	v_add_f32_e32 v45, v182, v95
	v_add_f32_e32 v32, v32, v33
	v_mul_f32_e32 v32, 0x3fb8aa3b, v32
	v_exp_f32_e32 v44, v32
	s_nop 15
	s_nop 15
	v_cvt_pk_bf16_f32 v32, v35, v34
	v_cvt_pk_bf16_f32 v33, v120, v122
	v_cvt_pk_bf16_f32 v35, v117, v116
	v_cvt_pk_bf16_f32 v34, v37, v36
	s_waitcnt vmcnt(17)
	v_perm_b32 v39, v154, v144, s38
	v_perm_b32 v38, v142, v139, s38
	v_perm_b32 v37, v93, v91, s38
	v_perm_b32 v36, v89, v85, s38
	v_add_f32_e32 v95, v45, v183
	s_nop 0
	v_mfma_f32_32x32x16_bf16 v[0:15], v[32:35], v[36:39], v[0:15]
	s_waitcnt vmcnt(16)
	v_perm_b32 v39, v140, v137, s38
	v_perm_b32 v38, v136, v97, s38
	v_perm_b32 v37, v87, v83, s38
	v_perm_b32 v36, v81, v79, s38
	s_nop 1
	v_mfma_f32_32x32x16_bf16 v[16:31], v[32:35], v[36:39], v[16:31]
	v_cvt_pk_bf16_f32 v32, v40, v42
	v_cvt_pk_bf16_f32 v33, v119, v118
	v_cvt_pk_bf16_f32 v34, v44, v46
	v_cvt_pk_bf16_f32 v35, v43, v41
	s_waitcnt vmcnt(1)
	v_perm_b32 v39, v165, v164, s38
	v_perm_b32 v38, v163, v161, s38
	v_perm_b32 v37, v157, v156, s38
	v_perm_b32 v36, v155, v152, s38
	s_nop 1
	v_mfma_f32_32x32x16_bf16 v[0:15], v[32:35], v[36:39], v[0:15]
	s_waitcnt vmcnt(0)
	v_perm_b32 v39, v162, v160, s38
	v_perm_b32 v38, v159, v158, s38
	v_perm_b32 v37, v153, v143, s38
	v_perm_b32 v36, v141, v138, s38
	s_nop 1
	v_mfma_f32_32x32x16_bf16 v[16:31], v[32:35], v[36:39], v[16:31]
	s_nop 15
	s_nop 15
	v_cmp_gt_f32_e32 vcc, s34, v95
	s_cmp_lg_u64 vcc, exec
	s_cselect_b64 s[6:7], -1, 0
	s_cmp_gt_u32 s22, 63
	s_mov_b32 s22, s10
	s_cselect_b64 s[10:11], -1, 0
	s_and_b64 s[6:7], s[10:11], s[6:7]
	v_lshl_add_u64 v[112:113], v[112:113], 0, s[24:25]
	v_lshl_add_u64 v[114:115], v[114:115], 0, s[24:25]
	s_and_b64 vcc, exec, s[6:7]
	s_cbranch_vccnz .LBB0_255
.LBB0_256:
	s_nop 3
	v_pk_mul_f32 v[44:45], v[16:17], v[16:17]
	v_pk_mul_f32 v[40:41], v[26:27], v[26:27]
	v_pk_fma_f32 v[44:45], v[0:1], v[0:1], v[44:45]
	ds_bpermute_b32 v46, v185, v44
	ds_bpermute_b32 v47, v185, v45
	v_pk_mul_f32 v[48:49], v[30:31], v[30:31]
	v_pk_mul_f32 v[42:43], v[28:29], v[28:29]
	v_pk_fma_f32 v[52:53], v[14:15], v[14:15], v[48:49]
	v_pk_fma_f32 v[48:49], v[10:11], v[10:11], v[40:41]
	s_waitcnt lgkmcnt(0)
	v_pk_add_f32 v[40:41], v[44:45], v[46:47]
	v_pk_fma_f32 v[54:55], v[12:13], v[12:13], v[42:43]
	s_nop 0
	v_mov_b32_dpp v42, v40 row_ror:8 row_mask:0xf bank_mask:0xf
	v_mov_b32_dpp v43, v41 row_ror:8 row_mask:0xf bank_mask:0xf
	v_pk_mul_f32 v[32:33], v[18:19], v[18:19]
	v_pk_mul_f32 v[38:39], v[24:25], v[24:25]
	v_pk_fma_f32 v[32:33], v[2:3], v[2:3], v[32:33]
	v_pk_fma_f32 v[44:45], v[8:9], v[8:9], v[38:39]
	s_waitcnt lgkmcnt(0)
	v_pk_add_f32 v[40:41], v[40:41], v[42:43]
	ds_bpermute_b32 v38, v185, v32
	ds_bpermute_b32 v39, v185, v33
	v_mov_b32_dpp v42, v40 row_half_mirror row_mask:0xf bank_mask:0xf
	s_nop 1
	v_mov_b32_dpp v42, v42 quad_perm:[3,2,1,0] row_mask:0xf bank_mask:0xf
	v_mov_b32_dpp v43, v41 row_half_mirror row_mask:0xf bank_mask:0xf
	s_nop 1
	v_mov_b32_dpp v43, v43 quad_perm:[3,2,1,0] row_mask:0xf bank_mask:0xf
	v_pk_mul_f32 v[36:37], v[22:23], v[22:23]
	v_pk_mul_f32 v[34:35], v[20:21], v[20:21]
	s_waitcnt lgkmcnt(0)
	v_pk_add_f32 v[32:33], v[32:33], v[38:39]
	v_pk_fma_f32 v[46:47], v[6:7], v[6:7], v[36:37]
	s_waitcnt lgkmcnt(0)
	v_pk_add_f32 v[38:39], v[40:41], v[42:43]
	v_mov_b32_dpp v36, v32 row_ror:8 row_mask:0xf bank_mask:0xf
	v_mov_b32_dpp v37, v33 row_ror:8 row_mask:0xf bank_mask:0xf
	v_mov_b32_dpp v40, v38 quad_perm:[2,3,0,1] row_mask:0xf bank_mask:0xf
	v_mov_b32_dpp v41, v39 quad_perm:[2,3,0,1] row_mask:0xf bank_mask:0xf
	v_pk_fma_f32 v[42:43], v[4:5], v[4:5], v[34:35]
	ds_bpermute_b32 v60, v185, v48
	s_waitcnt lgkmcnt(0)
	v_pk_add_f32 v[36:37], v[32:33], v[36:37]
	s_nop 1
	v_mov_b32_dpp v50, v36 row_half_mirror row_mask:0xf bank_mask:0xf
	s_nop 1
	v_mov_b32_dpp v50, v50 quad_perm:[3,2,1,0] row_mask:0xf bank_mask:0xf
	s_waitcnt lgkmcnt(0)
	v_pk_add_f32 v[32:33], v[38:39], v[40:41]
	ds_bpermute_b32 v38, v185, v42
	ds_bpermute_b32 v39, v185, v43
	v_mov_b32_dpp v51, v37 row_half_mirror row_mask:0xf bank_mask:0xf
	s_nop 1
	v_mov_b32_dpp v51, v51 quad_perm:[3,2,1,0] row_mask:0xf bank_mask:0xf
	ds_bpermute_b32 v61, v185, v49
	ds_bpermute_b32 v62, v185, v52
	ds_bpermute_b32 v63, v185, v53
	s_waitcnt lgkmcnt(0)
	v_pk_add_f32 v[38:39], v[42:43], v[38:39]
	s_waitcnt lgkmcnt(0)
	v_pk_add_f32 v[36:37], v[36:37], v[50:51]
	v_mov_b32_dpp v42, v38 row_ror:8 row_mask:0xf bank_mask:0xf
	v_mov_b32_dpp v43, v39 row_ror:8 row_mask:0xf bank_mask:0xf
	v_mov_b32_dpp v40, v36 quad_perm:[2,3,0,1] row_mask:0xf bank_mask:0xf
	v_mov_b32_dpp v41, v37 quad_perm:[2,3,0,1] row_mask:0xf bank_mask:0xf
	s_waitcnt lgkmcnt(0)
	v_pk_add_f32 v[48:49], v[48:49], v[60:61]
	s_waitcnt lgkmcnt(0)
	v_pk_add_f32 v[62:63], v[52:53], v[62:63]
	s_waitcnt lgkmcnt(0)
	v_pk_add_f32 v[42:43], v[38:39], v[42:43]
	s_nop 1
	v_mov_b32_dpp v50, v42 row_half_mirror row_mask:0xf bank_mask:0xf
	s_nop 1
	v_mov_b32_dpp v50, v50 quad_perm:[3,2,1,0] row_mask:0xf bank_mask:0xf
	s_waitcnt lgkmcnt(0)
	v_pk_add_f32 v[36:37], v[36:37], v[40:41]
	ds_bpermute_b32 v40, v185, v46
	ds_bpermute_b32 v41, v185, v47
	v_mov_b32_dpp v51, v43 row_half_mirror row_mask:0xf bank_mask:0xf
	s_nop 1
	v_mov_b32_dpp v51, v51 quad_perm:[3,2,1,0] row_mask:0xf bank_mask:0xf
	v_mov_b32_dpp v112, v62 row_ror:8 row_mask:0xf bank_mask:0xf
	v_mov_b32_dpp v113, v63 row_ror:8 row_mask:0xf bank_mask:0xf
	v_mov_b32_dpp v34, v32 quad_perm:[1,0,3,2] row_mask:0xf bank_mask:0xf
	s_waitcnt lgkmcnt(0)
	v_pk_add_f32 v[40:41], v[46:47], v[40:41]
	s_waitcnt lgkmcnt(0)
	v_pk_add_f32 v[42:43], v[42:43], v[50:51]
	v_mov_b32_dpp v46, v40 row_ror:8 row_mask:0xf bank_mask:0xf
	v_mov_b32_dpp v47, v41 row_ror:8 row_mask:0xf bank_mask:0xf
	v_mov_b32_dpp v50, v42 quad_perm:[2,3,0,1] row_mask:0xf bank_mask:0xf
	v_mov_b32_dpp v51, v43 quad_perm:[2,3,0,1] row_mask:0xf bank_mask:0xf
	v_mov_b32_dpp v35, v33 quad_perm:[1,0,3,2] row_mask:0xf bank_mask:0xf
	v_mov_b32_dpp v38, v36 quad_perm:[1,0,3,2] row_mask:0xf bank_mask:0xf
	s_waitcnt lgkmcnt(0)
	v_pk_add_f32 v[46:47], v[40:41], v[46:47]
	s_nop 1
	v_mov_b32_dpp v56, v46 row_half_mirror row_mask:0xf bank_mask:0xf
	s_nop 1
	v_mov_b32_dpp v56, v56 quad_perm:[3,2,1,0] row_mask:0xf bank_mask:0xf
	s_waitcnt lgkmcnt(0)
	v_pk_add_f32 v[40:41], v[42:43], v[50:51]
	ds_bpermute_b32 v50, v185, v44
	ds_bpermute_b32 v51, v185, v45
	v_mov_b32_dpp v57, v47 row_half_mirror row_mask:0xf bank_mask:0xf
	s_nop 1
	v_mov_b32_dpp v57, v57 quad_perm:[3,2,1,0] row_mask:0xf bank_mask:0xf
	v_mov_b32_dpp v39, v37 quad_perm:[1,0,3,2] row_mask:0xf bank_mask:0xf
	v_mov_b32_dpp v42, v40 quad_perm:[1,0,3,2] row_mask:0xf bank_mask:0xf
	v_mov_b32_dpp v43, v41 quad_perm:[1,0,3,2] row_mask:0xf bank_mask:0xf
	s_waitcnt lgkmcnt(0)
	v_pk_add_f32 v[50:51], v[44:45], v[50:51]
	s_waitcnt lgkmcnt(0)
	v_pk_add_f32 v[46:47], v[46:47], v[56:57]
	v_mov_b32_dpp v58, v50 row_ror:8 row_mask:0xf bank_mask:0xf
	v_mov_b32_dpp v59, v51 row_ror:8 row_mask:0xf bank_mask:0xf
	v_mov_b32_dpp v56, v46 quad_perm:[2,3,0,1] row_mask:0xf bank_mask:0xf
	v_mov_b32_dpp v57, v47 quad_perm:[2,3,0,1] row_mask:0xf bank_mask:0xf
	s_waitcnt lgkmcnt(0)
	s_barrier
	v_pk_add_f32 v[50:51], v[50:51], v[58:59]
	v_mov_b32_dpp v58, v48 row_ror:8 row_mask:0xf bank_mask:0xf
	v_pk_add_f32 v[44:45], v[46:47], v[56:57]
	v_mov_b32_dpp v56, v50 row_half_mirror row_mask:0xf bank_mask:0xf
	s_nop 1
	v_mov_b32_dpp v56, v56 quad_perm:[3,2,1,0] row_mask:0xf bank_mask:0xf
	v_mov_b32_dpp v57, v51 row_half_mirror row_mask:0xf bank_mask:0xf
	s_nop 1
	v_mov_b32_dpp v57, v57 quad_perm:[3,2,1,0] row_mask:0xf bank_mask:0xf
	v_mov_b32_dpp v59, v49 row_ror:8 row_mask:0xf bank_mask:0xf
	v_mov_b32_dpp v46, v44 quad_perm:[1,0,3,2] row_mask:0xf bank_mask:0xf
	v_mov_b32_dpp v47, v45 quad_perm:[1,0,3,2] row_mask:0xf bank_mask:0xf
	s_waitcnt lgkmcnt(0)
	v_pk_add_f32 v[50:51], v[50:51], v[56:57]
	v_pk_add_f32 v[58:59], v[48:49], v[58:59]
	s_nop 0
	v_mov_b32_dpp v56, v50 quad_perm:[2,3,0,1] row_mask:0xf bank_mask:0xf
	v_mov_b32_dpp v57, v51 quad_perm:[2,3,0,1] row_mask:0xf bank_mask:0xf
	v_mov_b32_dpp v60, v58 row_half_mirror row_mask:0xf bank_mask:0xf
	s_nop 1
	v_mov_b32_dpp v60, v60 quad_perm:[3,2,1,0] row_mask:0xf bank_mask:0xf
	v_mov_b32_dpp v61, v59 row_half_mirror row_mask:0xf bank_mask:0xf
	s_nop 1
	v_mov_b32_dpp v61, v61 quad_perm:[3,2,1,0] row_mask:0xf bank_mask:0xf
	s_waitcnt lgkmcnt(0)
	v_pk_add_f32 v[48:49], v[50:51], v[56:57]
	s_nop 1
	v_mov_b32_dpp v50, v48 quad_perm:[1,0,3,2] row_mask:0xf bank_mask:0xf
	s_waitcnt lgkmcnt(0)
	v_pk_add_f32 v[56:57], v[58:59], v[60:61]
	ds_bpermute_b32 v58, v185, v54
	ds_bpermute_b32 v59, v185, v55
	v_mov_b32_dpp v60, v56 quad_perm:[2,3,0,1] row_mask:0xf bank_mask:0xf
	v_mov_b32_dpp v61, v57 quad_perm:[2,3,0,1] row_mask:0xf bank_mask:0xf
	v_mov_b32_dpp v51, v49 quad_perm:[1,0,3,2] row_mask:0xf bank_mask:0xf
	s_waitcnt lgkmcnt(0)
	v_pk_add_f32 v[54:55], v[54:55], v[58:59]
	s_nop 1
	v_mov_b32_dpp v58, v54 row_ror:8 row_mask:0xf bank_mask:0xf
	s_nop 0
	v_mov_b32_dpp v59, v55 row_ror:8 row_mask:0xf bank_mask:0xf
	s_waitcnt lgkmcnt(0)
	v_pk_add_f32 v[52:53], v[56:57], v[60:61]
	v_pk_add_f32 v[60:61], v[62:63], v[112:113]
	s_nop 1
	v_mov_b32_dpp v62, v60 row_half_mirror row_mask:0xf bank_mask:0xf
	s_nop 1
	v_mov_b32_dpp v62, v62 quad_perm:[3,2,1,0] row_mask:0xf bank_mask:0xf
	v_mov_b32_dpp v63, v61 row_half_mirror row_mask:0xf bank_mask:0xf
	s_nop 1
	v_mov_b32_dpp v63, v63 quad_perm:[3,2,1,0] row_mask:0xf bank_mask:0xf
	s_waitcnt lgkmcnt(0)
	v_pk_add_f32 v[56:57], v[54:55], v[58:59]
	s_nop 1
	v_mov_b32_dpp v58, v56 row_half_mirror row_mask:0xf bank_mask:0xf
	s_nop 1
	v_mov_b32_dpp v58, v58 quad_perm:[3,2,1,0] row_mask:0xf bank_mask:0xf
	v_mov_b32_dpp v59, v57 row_half_mirror row_mask:0xf bank_mask:0xf
	s_nop 1
	v_mov_b32_dpp v59, v59 quad_perm:[3,2,1,0] row_mask:0xf bank_mask:0xf
	v_mov_b32_dpp v54, v52 quad_perm:[1,0,3,2] row_mask:0xf bank_mask:0xf
	s_waitcnt lgkmcnt(0)
	v_pk_add_f32 v[60:61], v[60:61], v[62:63]
	s_nop 1
	v_mov_b32_dpp v62, v60 quad_perm:[2,3,0,1] row_mask:0xf bank_mask:0xf
	s_nop 0
	v_mov_b32_dpp v63, v61 quad_perm:[2,3,0,1] row_mask:0xf bank_mask:0xf
	s_waitcnt lgkmcnt(0)
	v_pk_add_f32 v[56:57], v[56:57], v[58:59]
	s_nop 1
	v_mov_b32_dpp v58, v56 quad_perm:[2,3,0,1] row_mask:0xf bank_mask:0xf
	s_nop 0
	v_mov_b32_dpp v59, v57 quad_perm:[2,3,0,1] row_mask:0xf bank_mask:0xf
	v_mov_b32_dpp v55, v53 quad_perm:[1,0,3,2] row_mask:0xf bank_mask:0xf
	s_waitcnt lgkmcnt(0)
	v_pk_add_f32 v[60:61], v[60:61], v[62:63]
	s_nop 1
	v_mov_b32_dpp v62, v60 quad_perm:[1,0,3,2] row_mask:0xf bank_mask:0xf
	s_nop 0
	v_mov_b32_dpp v63, v61 quad_perm:[1,0,3,2] row_mask:0xf bank_mask:0xf
	s_waitcnt lgkmcnt(0)
	v_pk_add_f32 v[56:57], v[56:57], v[58:59]
	s_nop 1
	v_mov_b32_dpp v58, v56 quad_perm:[1,0,3,2] row_mask:0xf bank_mask:0xf
	s_nop 0
	v_mov_b32_dpp v59, v57 quad_perm:[1,0,3,2] row_mask:0xf bank_mask:0xf
	s_and_saveexec_b64 s[6:7], s[44:45]
	s_cbranch_execz .LBB0_258
	v_pk_add_f32 v[32:33], v[32:33], v[34:35]
	v_pk_add_f32 v[34:35], v[36:37], v[38:39]
	ds_write_b128 v77, v[32:35]
	v_pk_add_f32 v[32:33], v[40:41], v[42:43]
	v_pk_add_f32 v[34:35], v[44:45], v[46:47]
	ds_write_b128 v77, v[32:35] offset:32
	v_pk_add_f32 v[32:33], v[48:49], v[50:51]
	s_waitcnt lgkmcnt(0)
	v_pk_add_f32 v[34:35], v[52:53], v[54:55]
	ds_write_b128 v77, v[32:35] offset:64
	s_waitcnt lgkmcnt(0)
	v_pk_add_f32 v[32:33], v[56:57], v[58:59]
	v_pk_add_f32 v[34:35], v[60:61], v[62:63]
	ds_write_b128 v77, v[32:35] offset:96
